# v037 + non-temporal hint on the P0 f32 weight LDS-DMA reads (read-once stream)
# speedup vs baseline: 1.0005x; 1.0005x over previous
.LBB0_33:
	s_andn2_b64 vcc, exec, s[0:1]
	s_cbranch_vccnz .LBB0_65
	v_lshlrev_b32_e32 v8, 2, v0
	v_and_b32_e32 v1, 28, v8
	v_add_u32_e32 v2, s71, v1
	s_add_i32 s0, s20, -4
	v_lshrrev_b32_e32 v72, 3, v0
	v_min_u32_e32 v4, s0, v2
	v_mul_u32_u24_e32 v2, s20, v72
	v_readlane_b32 s0, v252, 46
	s_mov_b32 s15, 0
	v_lshlrev_b32_e32 v2, 2, v2
	v_mov_b32_e32 v3, 0
	s_lshl_b32 s0, s0, 10
	s_mov_b32 s21, s15
	v_lshl_add_u64 v[6:7], s[2:3], 0, v[2:3]
	v_mov_b32_e32 v5, v3
	s_add_i32 s30, s0, 0
	v_lshl_add_u64 v[4:5], v[4:5], 2, v[6:7]
	s_mov_b32 m0, s30
	s_lshl_b64 s[0:1], s[20:21], 8
	s_add_i32 s21, s30, 0x2000
	global_load_lds_dwordx4 v[4:5], off nt
	v_lshl_add_u64 v[4:5], v[4:5], 0, s[0:1]
	s_mov_b32 m0, s21
	s_add_i32 s31, s30, 0x4000
	global_load_lds_dwordx4 v[4:5], off nt
	v_lshl_add_u64 v[4:5], v[4:5], 0, s[0:1]
	s_mov_b32 m0, s31
	s_add_i32 s34, s30, 0x6000
	global_load_lds_dwordx4 v[4:5], off nt
	v_lshl_add_u64 v[4:5], v[4:5], 0, s[0:1]
	s_mov_b32 m0, s34
	s_add_i32 s35, s30, 0x8000
	global_load_lds_dwordx4 v[4:5], off nt
	v_lshl_add_u64 v[4:5], v[4:5], 0, s[0:1]
	s_mov_b32 m0, s35
	s_add_i32 s36, s30, 0xa000
	global_load_lds_dwordx4 v[4:5], off nt
	v_lshl_add_u64 v[4:5], v[4:5], 0, s[0:1]
	s_mov_b32 m0, s36
	s_add_i32 s37, s30, 0xc000
	global_load_lds_dwordx4 v[4:5], off nt
	v_lshl_add_u64 v[4:5], v[4:5], 0, s[0:1]
	s_mov_b32 m0, s37
	s_add_i32 s42, s30, 0xe000
	global_load_lds_dwordx4 v[4:5], off nt
	v_lshl_add_u64 v[4:5], v[4:5], 0, s[0:1]
	s_mov_b32 m0, s42
	s_add_i32 s43, s30, 0x10000
	global_load_lds_dwordx4 v[4:5], off nt
	v_lshl_add_u64 v[4:5], v[4:5], 0, s[0:1]
	s_mov_b32 m0, s43
	s_add_i32 s45, s30, 0x12000
	global_load_lds_dwordx4 v[4:5], off nt
	v_lshl_add_u64 v[4:5], v[4:5], 0, s[0:1]
	s_mov_b32 m0, s45
	s_add_i32 s46, s30, 0x14000
	global_load_lds_dwordx4 v[4:5], off nt
	v_lshl_add_u64 v[4:5], v[4:5], 0, s[0:1]
	s_mov_b32 m0, s46
	s_add_i32 s47, s30, 0x16000
	global_load_lds_dwordx4 v[4:5], off nt
	v_lshl_add_u64 v[4:5], v[4:5], 0, s[0:1]
	s_mov_b32 m0, s47
	s_add_i32 s48, s30, 0x18000
	global_load_lds_dwordx4 v[4:5], off nt
	v_lshl_add_u64 v[4:5], v[4:5], 0, s[0:1]
	s_mov_b32 m0, s48
	s_add_i32 s49, s30, 0x1a000
	global_load_lds_dwordx4 v[4:5], off nt
	v_lshl_add_u64 v[4:5], v[4:5], 0, s[0:1]
	s_mov_b32 m0, s49
	s_add_i32 s50, s30, 0x1c000
	global_load_lds_dwordx4 v[4:5], off nt
	v_lshl_add_u64 v[4:5], v[4:5], 0, s[0:1]
	s_mov_b32 m0, s50
	s_add_i32 s51, s30, 0x1e000
	global_load_lds_dwordx4 v[4:5], off nt
	v_lshl_add_u64 v[4:5], v[4:5], 0, s[0:1]
	s_mov_b32 m0, s51
	v_readlane_b32 s0, v252, 53
	global_load_lds_dwordx4 v[4:5], off nt
	v_readlane_b32 s1, v252, 54
	s_add_u32 s54, s0, 0x685000
	s_addc_u32 s55, s1, 0
	s_add_u32 s18, s0, 0x603000
	s_addc_u32 s19, s1, 0
	v_and_b32_e32 v73, 31, v0
	v_lshrrev_b32_e32 v2, 5, v0
	s_add_u32 s56, s0, 0x605000
	v_lshlrev_b32_e32 v4, 13, v2
	v_lshlrev_b32_e32 v5, 2, v73
	s_addc_u32 s57, s1, 0
	v_add3_u32 v74, 0, v4, v5
	s_add_i32 s0, 0, 0x20400
	s_mov_b32 s93, s65
	v_add_u32_e32 v75, s0, v8
	v_cmp_lt_u32_e64 s[2:3], 31, v0
	v_add_u32_e32 v76, s0, v5
	v_lshlrev_b32_e32 v4, 6, v2
	v_mov_b32_e32 v5, v3
	s_mov_b32 s63, 1
	s_mov_b32 s64, 0x42fe0000
	s_mov_b32 s65, 0x40c0c00
	s_mov_b32 s66, 0x43c00000
	v_add_u32_e32 v77, 0x400, v74
	v_add_u32_e32 v78, 0x800, v74
	v_add_u32_e32 v79, 0xc00, v74
	v_add_u32_e32 v80, 0x1000, v74
	v_add_u32_e32 v81, 0x1400, v74
	v_add_u32_e32 v82, 0x1800, v74
	v_add_u32_e32 v83, 0x1c00, v74
	s_branch .LBB0_37

.LBB0_51:
	v_add_u32_e32 v84, s71, v73
	v_cndmask_b32_e64 v2, 0, 1, s[0:1]
	s_mov_b64 s[28:29], -1
	s_cmp_lg_u32 s72, 2
	v_cmp_gt_u32_e32 vcc, s20, v84
	v_cmp_ne_u32_e64 s[0:1], 1, v2
	s_cbranch_scc0 .LBB0_57
	s_waitcnt vmcnt(0)
	s_barrier
	ds_read2_b32 v[70:71], v74 offset1:32
	ds_read2_b32 v[68:69], v74 offset0:64 offset1:96
	ds_read2_b32 v[66:67], v74 offset0:128 offset1:160
	ds_read2_b32 v[64:65], v74 offset0:192 offset1:224
	ds_read2_b32 v[62:63], v77 offset1:32
	ds_read2_b32 v[60:61], v77 offset0:64 offset1:96
	ds_read2_b32 v[56:57], v77 offset0:128 offset1:160
	ds_read2_b32 v[58:59], v77 offset0:192 offset1:224
	ds_read2_b32 v[54:55], v78 offset1:32
	ds_read2_b32 v[52:53], v78 offset0:64 offset1:96
	ds_read2_b32 v[50:51], v78 offset0:128 offset1:160
	ds_read2_b32 v[48:49], v78 offset0:192 offset1:224
	ds_read2_b32 v[46:47], v79 offset1:32
	ds_read2_b32 v[44:45], v79 offset0:64 offset1:96
	ds_read2_b32 v[40:41], v79 offset0:128 offset1:160
	ds_read2_b32 v[38:39], v79 offset0:192 offset1:224
	ds_read2_b32 v[34:35], v80 offset1:32
	s_waitcnt lgkmcnt(14)
	v_max3_f32 v2, |v70|, 0, |v71|
	v_max3_f32 v2, v2, |v68|, |v69|
	v_max3_f32 v2, v2, |v66|, |v67|
	s_waitcnt lgkmcnt(13)
	v_max3_f32 v2, v2, |v64|, |v65|
	s_waitcnt lgkmcnt(12)
	v_max3_f32 v2, v2, |v62|, |v63|
	s_waitcnt lgkmcnt(11)
	v_max3_f32 v2, v2, |v60|, |v61|
	s_waitcnt lgkmcnt(10)
	v_max3_f32 v2, v2, |v56|, |v57|
	s_waitcnt lgkmcnt(9)
	v_max3_f32 v2, v2, |v58|, |v59|
	s_waitcnt lgkmcnt(8)
	v_max3_f32 v2, v2, |v54|, |v55|
	s_waitcnt lgkmcnt(7)
	v_max3_f32 v2, v2, |v52|, |v53|
	s_waitcnt lgkmcnt(6)
	v_max3_f32 v2, v2, |v50|, |v51|
	s_waitcnt lgkmcnt(5)
	v_max3_f32 v2, v2, |v48|, |v49|
	s_waitcnt lgkmcnt(4)
	v_max3_f32 v2, v2, |v46|, |v47|
	s_waitcnt lgkmcnt(3)
	v_max3_f32 v2, v2, |v44|, |v45|
	s_waitcnt lgkmcnt(2)
	v_max3_f32 v2, v2, |v40|, |v41|
	s_waitcnt lgkmcnt(1)
	v_max3_f32 v2, v2, |v38|, |v39|
	s_waitcnt lgkmcnt(0)
	v_max3_f32 v2, v2, |v34|, |v35|
	ds_read2_b32 v[36:37], v80 offset0:64 offset1:96
	ds_read2_b32 v[32:33], v80 offset0:128 offset1:160
	ds_read2_b32 v[30:31], v80 offset0:192 offset1:224
	ds_read2_b32 v[28:29], v81 offset1:32
	ds_read2_b32 v[26:27], v81 offset0:64 offset1:96
	s_waitcnt lgkmcnt(4)
	v_max3_f32 v2, v2, |v36|, |v37|
	s_waitcnt lgkmcnt(3)
	v_max3_f32 v2, v2, |v32|, |v33|
	s_waitcnt lgkmcnt(2)
	v_max3_f32 v2, v2, |v30|, |v31|
	s_waitcnt lgkmcnt(1)
	v_max3_f32 v2, v2, |v28|, |v29|
	s_waitcnt lgkmcnt(0)
	v_max3_f32 v2, v2, |v26|, |v27|
	ds_read2_b32 v[24:25], v81 offset0:128 offset1:160
	ds_read2_b32 v[22:23], v81 offset0:192 offset1:224
	ds_read2_b32 v[20:21], v82 offset1:32
	ds_read2_b32 v[18:19], v82 offset0:64 offset1:96
	ds_read2_b32 v[14:15], v82 offset0:128 offset1:160
	s_waitcnt lgkmcnt(4)
	v_max3_f32 v2, v2, |v24|, |v25|
	s_waitcnt lgkmcnt(3)
	v_max3_f32 v2, v2, |v22|, |v23|
	s_waitcnt lgkmcnt(2)
	v_max3_f32 v2, v2, |v20|, |v21|
	s_waitcnt lgkmcnt(1)
	v_max3_f32 v2, v2, |v18|, |v19|
	s_waitcnt lgkmcnt(0)
	v_max3_f32 v2, v2, |v14|, |v15|
	ds_read2_b32 v[16:17], v82 offset0:192 offset1:224
	ds_read2_b32 v[12:13], v83 offset1:32
	ds_read2_b32 v[10:11], v83 offset0:64 offset1:96
	ds_read2_b32 v[8:9], v83 offset0:128 offset1:160
	ds_read2_b32 v[6:7], v83 offset0:192 offset1:224
	s_waitcnt lgkmcnt(4)
	v_max3_f32 v2, v2, |v16|, |v17|
	s_waitcnt lgkmcnt(3)
	v_max3_f32 v2, v2, |v12|, |v13|
	s_waitcnt lgkmcnt(2)
	v_max3_f32 v2, v2, |v10|, |v11|
	s_waitcnt lgkmcnt(1)
	v_max3_f32 v2, v2, |v8|, |v9|
	s_waitcnt lgkmcnt(0)
	v_max3_f32 v2, v2, |v6|, |v7|
	v_cndmask_b32_e32 v2, 0, v2, vcc
	ds_write_b32 v75, v2
	s_waitcnt lgkmcnt(0)
	s_and_b64 vcc, exec, s[0:1]
	s_waitcnt lgkmcnt(0)
	s_barrier
	s_cbranch_vccnz .LBB0_54
	v_add_u32_e32 v2, s68, v1
	s_add_i32 s28, s14, -4
	v_min_u32_e32 v42, s28, v2
	v_mul_u32_u24_e32 v2, s14, v72
	v_lshlrev_b32_e32 v2, 2, v2
	v_lshl_add_u64 v[86:87], s[26:27], 0, v[2:3]
	v_mov_b32_e32 v43, v3
	s_mov_b32 m0, s30
	v_lshl_add_u64 v[42:43], v[42:43], 2, v[86:87]
	s_lshl_b64 s[28:29], s[14:15], 8
	global_load_lds_dwordx4 v[42:43], off nt
	v_lshl_add_u64 v[42:43], v[42:43], 0, s[28:29]
	s_mov_b32 m0, s21
	s_nop 0
	global_load_lds_dwordx4 v[42:43], off nt
	v_lshl_add_u64 v[42:43], v[42:43], 0, s[28:29]
	s_mov_b32 m0, s31
	s_nop 0
	global_load_lds_dwordx4 v[42:43], off nt
	v_lshl_add_u64 v[42:43], v[42:43], 0, s[28:29]
	s_mov_b32 m0, s34
	s_nop 0
	global_load_lds_dwordx4 v[42:43], off nt
	v_lshl_add_u64 v[42:43], v[42:43], 0, s[28:29]
	s_mov_b32 m0, s35
	s_nop 0
	global_load_lds_dwordx4 v[42:43], off nt
	v_lshl_add_u64 v[42:43], v[42:43], 0, s[28:29]
	s_mov_b32 m0, s36
	s_nop 0
	global_load_lds_dwordx4 v[42:43], off nt
	v_lshl_add_u64 v[42:43], v[42:43], 0, s[28:29]
	s_mov_b32 m0, s37
	s_nop 0
	global_load_lds_dwordx4 v[42:43], off nt
	v_lshl_add_u64 v[42:43], v[42:43], 0, s[28:29]
	s_mov_b32 m0, s42
	s_nop 0
	global_load_lds_dwordx4 v[42:43], off nt
	v_lshl_add_u64 v[42:43], v[42:43], 0, s[28:29]
	s_mov_b32 m0, s43
	s_nop 0
	global_load_lds_dwordx4 v[42:43], off nt
	v_lshl_add_u64 v[42:43], v[42:43], 0, s[28:29]
	s_mov_b32 m0, s45
	s_nop 0
	global_load_lds_dwordx4 v[42:43], off nt
	v_lshl_add_u64 v[42:43], v[42:43], 0, s[28:29]
	s_mov_b32 m0, s46
	s_nop 0
	global_load_lds_dwordx4 v[42:43], off nt
	v_lshl_add_u64 v[42:43], v[42:43], 0, s[28:29]
	s_mov_b32 m0, s47
	s_nop 0
	global_load_lds_dwordx4 v[42:43], off nt
	v_lshl_add_u64 v[42:43], v[42:43], 0, s[28:29]
	s_mov_b32 m0, s48
	s_nop 0
	global_load_lds_dwordx4 v[42:43], off nt
	v_lshl_add_u64 v[42:43], v[42:43], 0, s[28:29]
	s_mov_b32 m0, s49
	s_nop 0
	global_load_lds_dwordx4 v[42:43], off nt
	v_lshl_add_u64 v[42:43], v[42:43], 0, s[28:29]
	s_mov_b32 m0, s50
	s_nop 0
	global_load_lds_dwordx4 v[42:43], off nt
	v_lshl_add_u64 v[42:43], v[42:43], 0, s[28:29]
	s_mov_b32 m0, s51
	s_nop 0
	global_load_lds_dwordx4 v[42:43], off nt

.LBB0_57:
	s_and_b64 vcc, exec, s[28:29]
	s_cbranch_vccz .LBB0_36
	s_waitcnt vmcnt(0)
	s_barrier
	ds_read2_b32 v[68:69], v74 offset1:32
	ds_read2_b32 v[66:67], v74 offset0:64 offset1:96
	ds_read2_b32 v[64:65], v74 offset0:128 offset1:160
	ds_read2_b32 v[62:63], v74 offset0:192 offset1:224
	ds_read2_b32 v[60:61], v77 offset1:32
	ds_read2_b32 v[58:59], v77 offset0:64 offset1:96
	ds_read2_b32 v[56:57], v77 offset0:128 offset1:160
	ds_read2_b32 v[54:55], v77 offset0:192 offset1:224
	ds_read2_b32 v[52:53], v78 offset1:32
	ds_read2_b32 v[50:51], v78 offset0:64 offset1:96
	ds_read2_b32 v[48:49], v78 offset0:128 offset1:160
	ds_read2_b32 v[44:45], v78 offset0:192 offset1:224
	ds_read2_b32 v[40:41], v79 offset1:32
	s_waitcnt lgkmcnt(12)
	v_max3_f32 v2, |v68|, 0, |v69|
	s_waitcnt lgkmcnt(11)
	v_max3_f32 v2, v2, |v66|, |v67|
	s_waitcnt lgkmcnt(10)
	v_max3_f32 v2, v2, |v64|, |v65|
	s_waitcnt lgkmcnt(9)
	v_max3_f32 v2, v2, |v62|, |v63|
	s_waitcnt lgkmcnt(8)
	v_max3_f32 v2, v2, |v60|, |v61|
	s_waitcnt lgkmcnt(7)
	v_max3_f32 v2, v2, |v58|, |v59|
	s_waitcnt lgkmcnt(6)
	v_max3_f32 v2, v2, |v56|, |v57|
	s_waitcnt lgkmcnt(5)
	v_max3_f32 v2, v2, |v54|, |v55|
	s_waitcnt lgkmcnt(4)
	v_max3_f32 v2, v2, |v52|, |v53|
	s_waitcnt lgkmcnt(3)
	v_max3_f32 v2, v2, |v50|, |v51|
	s_waitcnt lgkmcnt(2)
	v_max3_f32 v2, v2, |v48|, |v49|
	s_waitcnt lgkmcnt(1)
	v_max3_f32 v2, v2, |v44|, |v45|
	s_waitcnt lgkmcnt(0)
	v_max3_f32 v2, v2, |v40|, |v41|
	ds_read2_b32 v[46:47], v79 offset0:64 offset1:96
	ds_read2_b32 v[42:43], v79 offset0:128 offset1:160
	ds_read2_b32 v[38:39], v79 offset0:192 offset1:224
	ds_read2_b32 v[34:35], v80 offset1:32
	ds_read2_b32 v[32:33], v80 offset0:64 offset1:96
	s_waitcnt lgkmcnt(4)
	v_max3_f32 v2, v2, |v46|, |v47|
	s_waitcnt lgkmcnt(3)
	v_max3_f32 v2, v2, |v42|, |v43|
	s_waitcnt lgkmcnt(2)
	v_max3_f32 v2, v2, |v38|, |v39|
	s_waitcnt lgkmcnt(1)
	v_max3_f32 v2, v2, |v34|, |v35|
	s_waitcnt lgkmcnt(0)
	v_max3_f32 v2, v2, |v32|, |v33|
	ds_read2_b32 v[36:37], v80 offset0:128 offset1:160
	ds_read2_b32 v[30:31], v80 offset0:192 offset1:224
	ds_read2_b32 v[28:29], v81 offset1:32
	ds_read2_b32 v[26:27], v81 offset0:64 offset1:96
	ds_read2_b32 v[22:23], v81 offset0:128 offset1:160
	s_waitcnt lgkmcnt(4)
	v_max3_f32 v2, v2, |v36|, |v37|
	s_waitcnt lgkmcnt(3)
	v_max3_f32 v2, v2, |v30|, |v31|
	s_waitcnt lgkmcnt(2)
	v_max3_f32 v2, v2, |v28|, |v29|
	s_waitcnt lgkmcnt(1)
	v_max3_f32 v2, v2, |v26|, |v27|
	s_waitcnt lgkmcnt(0)
	v_max3_f32 v2, v2, |v22|, |v23|
	ds_read2_b32 v[24:25], v81 offset0:192 offset1:224
	ds_read2_b32 v[20:21], v82 offset1:32
	ds_read2_b32 v[18:19], v82 offset0:64 offset1:96
	ds_read2_b32 v[16:17], v82 offset0:128 offset1:160
	ds_read2_b32 v[10:11], v82 offset0:192 offset1:224
	s_waitcnt lgkmcnt(4)
	v_max3_f32 v2, v2, |v24|, |v25|
	s_waitcnt lgkmcnt(3)
	v_max3_f32 v2, v2, |v20|, |v21|
	s_waitcnt lgkmcnt(2)
	v_max3_f32 v2, v2, |v18|, |v19|
	s_waitcnt lgkmcnt(1)
	v_max3_f32 v2, v2, |v16|, |v17|
	ds_read2_b32 v[14:15], v83 offset1:32
	ds_read2_b32 v[12:13], v83 offset0:64 offset1:96
	ds_read2_b32 v[8:9], v83 offset0:128 offset1:160
	ds_read2_b32 v[6:7], v83 offset0:192 offset1:224
	s_waitcnt lgkmcnt(4)
	v_max3_f32 v2, v2, |v10|, |v11|
	s_waitcnt lgkmcnt(3)
	v_max3_f32 v2, v2, |v14|, |v15|
	s_waitcnt lgkmcnt(2)
	v_max3_f32 v2, v2, |v12|, |v13|
	s_waitcnt lgkmcnt(1)
	v_max3_f32 v2, v2, |v8|, |v9|
	s_waitcnt lgkmcnt(0)
	v_max3_f32 v2, v2, |v6|, |v7|
	v_cmp_gt_u32_e32 vcc, s20, v84
	s_nop 1
	v_cndmask_b32_e32 v2, 0, v2, vcc
	ds_write_b32 v75, v2
	s_waitcnt lgkmcnt(0)
	s_and_b64 vcc, exec, s[0:1]
	s_waitcnt lgkmcnt(0)
	s_barrier
	s_cbranch_vccnz .LBB0_60
	v_add_u32_e32 v2, s68, v1
	s_add_i32 s0, s14, -4
	v_min_u32_e32 v70, s0, v2
	v_mul_u32_u24_e32 v2, s14, v72
	v_lshlrev_b32_e32 v2, 2, v2
	v_lshl_add_u64 v[86:87], s[26:27], 0, v[2:3]
	v_mov_b32_e32 v71, v3
	s_mov_b32 m0, s30
	v_lshl_add_u64 v[70:71], v[70:71], 2, v[86:87]
	s_lshl_b64 s[0:1], s[14:15], 8
	global_load_lds_dwordx4 v[70:71], off nt
	v_lshl_add_u64 v[70:71], v[70:71], 0, s[0:1]
	s_mov_b32 m0, s21
	s_nop 0
	global_load_lds_dwordx4 v[70:71], off nt
	v_lshl_add_u64 v[70:71], v[70:71], 0, s[0:1]
	s_mov_b32 m0, s31
	s_nop 0
	global_load_lds_dwordx4 v[70:71], off nt
	v_lshl_add_u64 v[70:71], v[70:71], 0, s[0:1]
	s_mov_b32 m0, s34
	s_nop 0
	global_load_lds_dwordx4 v[70:71], off nt
	v_lshl_add_u64 v[70:71], v[70:71], 0, s[0:1]
	s_mov_b32 m0, s35
	s_nop 0
	global_load_lds_dwordx4 v[70:71], off nt
	v_lshl_add_u64 v[70:71], v[70:71], 0, s[0:1]
	s_mov_b32 m0, s36
	s_nop 0
	global_load_lds_dwordx4 v[70:71], off nt
	v_lshl_add_u64 v[70:71], v[70:71], 0, s[0:1]
	s_mov_b32 m0, s37
	s_nop 0
	global_load_lds_dwordx4 v[70:71], off nt
	v_lshl_add_u64 v[70:71], v[70:71], 0, s[0:1]
	s_mov_b32 m0, s42
	s_nop 0
	global_load_lds_dwordx4 v[70:71], off nt
	v_lshl_add_u64 v[70:71], v[70:71], 0, s[0:1]
	s_mov_b32 m0, s43
	s_nop 0
	global_load_lds_dwordx4 v[70:71], off nt
	v_lshl_add_u64 v[70:71], v[70:71], 0, s[0:1]
	s_mov_b32 m0, s45
	s_nop 0
	global_load_lds_dwordx4 v[70:71], off nt
	v_lshl_add_u64 v[70:71], v[70:71], 0, s[0:1]
	s_mov_b32 m0, s46
	s_nop 0
	global_load_lds_dwordx4 v[70:71], off nt
	v_lshl_add_u64 v[70:71], v[70:71], 0, s[0:1]
	s_mov_b32 m0, s47
	s_nop 0
	global_load_lds_dwordx4 v[70:71], off nt
	v_lshl_add_u64 v[70:71], v[70:71], 0, s[0:1]
	s_mov_b32 m0, s48
	s_nop 0
	global_load_lds_dwordx4 v[70:71], off nt
	v_lshl_add_u64 v[70:71], v[70:71], 0, s[0:1]
	s_mov_b32 m0, s49
	s_nop 0
	global_load_lds_dwordx4 v[70:71], off nt
	v_lshl_add_u64 v[70:71], v[70:71], 0, s[0:1]
	s_mov_b32 m0, s50
	s_nop 0
	global_load_lds_dwordx4 v[70:71], off nt
	v_lshl_add_u64 v[70:71], v[70:71], 0, s[0:1]
	s_mov_b32 m0, s51
	s_nop 0
	global_load_lds_dwordx4 v[70:71], off nt
